# up-GEMM: next-unit rowmap loads no longer drained (vmcnt(0)) before the K-loop; offsets formed in the last K-iteration header
# speedup vs baseline: 1.0196x; 1.0010x over previous
.LBB0_1088:
	v_readlane_b32 s30, v254, 32
	v_mov_b32_e32 v173, v113
	v_mov_b32_e32 v175, v113
	v_readlane_b32 s31, v254, 33
	s_add_u32 s37, s40, 0x100
	v_lshl_add_u64 v[176:177], s[30:31], 0, v[174:175]
	v_lshl_add_u64 v[178:179], s[30:31], 0, v[172:173]
	s_addc_u32 s47, s41, 0
	s_mov_b32 s49, -2
	s_mov_b64 s[72:73], 0
	v_mov_b32_e32 v173, v168
	v_mov_b32_e32 v175, v170
	v_mov_b32_e32 v217, v172
	v_mov_b32_e32 v218, v174
	s_cmpk_eq_i32 s72, 0x300
	s_cselect_b64 s[40:41], -1, 0
	s_and_b64 s[30:31], s[70:71], s[40:41]
	s_andn2_b64 vcc, exec, s[30:31]
	s_cbranch_vccnz .Lpeel_up_body
	s_waitcnt vmcnt(0)
	v_lshlrev_b32_e32 v0, 8, v171
	v_cmp_lt_i32_e32 vcc, -1, v171
	v_and_b32_e32 v0, 0xfffffc00, v0
	s_nop 0
	v_cndmask_b32_e32 v0, 0, v0, vcc
	v_add_u32_e32 v167, v0, v191
	v_lshlrev_b32_e32 v0, 8, v195
	v_cmp_lt_i32_e32 vcc, -1, v195
	v_and_b32_e32 v0, 0xfffffc00, v0
	s_nop 0
	v_cndmask_b32_e32 v0, 0, v0, vcc
	v_add_u32_e32 v220, v0, v192
	v_lshlrev_b32_e32 v0, 8, v215
	v_cmp_lt_i32_e32 vcc, -1, v215
	v_and_b32_e32 v0, 0xfffffc00, v0
	s_nop 0
	v_cndmask_b32_e32 v0, 0, v0, vcc
	v_add_u32_e32 v221, v0, v191
	v_lshlrev_b32_e32 v0, 8, v216
	v_cmp_lt_i32_e32 vcc, -1, v216
	v_and_b32_e32 v0, 0xfffffc00, v0
	s_nop 0
	v_cndmask_b32_e32 v0, 0, v0, vcc
	v_add_u32_e32 v222, v0, v192
	v_mov_b32_e32 v173, v167
	v_mov_b32_e32 v175, v220
	v_mov_b32_e32 v217, v221
	v_mov_b32_e32 v218, v222

.LBB0_1090:
	s_cmpk_eq_i32 s72, 0x300
	s_cselect_b64 s[40:41], -1, 0
	s_and_b64 s[30:31], s[70:71], s[40:41]
	s_andn2_b64 vcc, exec, s[30:31]
	s_cbranch_vccnz .LBB0_1089
	v_lshlrev_b32_e32 v0, 8, v171
	v_cmp_lt_i32_e32 vcc, -1, v171
	v_and_b32_e32 v0, 0xfffffc00, v0
	s_nop 0
	v_cndmask_b32_e32 v0, 0, v0, vcc
	v_add_u32_e32 v167, v0, v191
	v_lshlrev_b32_e32 v0, 8, v195
	v_cmp_lt_i32_e32 vcc, -1, v195
	v_and_b32_e32 v0, 0xfffffc00, v0
	s_nop 0
	v_cndmask_b32_e32 v0, 0, v0, vcc
	v_add_u32_e32 v220, v0, v192
	v_lshlrev_b32_e32 v0, 8, v215
	v_cmp_lt_i32_e32 vcc, -1, v215
	v_and_b32_e32 v0, 0xfffffc00, v0
	s_nop 0
	v_cndmask_b32_e32 v0, 0, v0, vcc
	v_add_u32_e32 v221, v0, v191
	v_lshlrev_b32_e32 v0, 8, v216
	v_cmp_lt_i32_e32 vcc, -1, v216
	v_and_b32_e32 v0, 0xfffffc00, v0
	s_nop 0
	v_cndmask_b32_e32 v0, 0, v0, vcc
	v_add_u32_e32 v222, v0, v192
	v_mov_b32_e32 v173, v167
	v_mov_b32_e32 v175, v220
	v_mov_b32_e32 v217, v221
	v_mov_b32_e32 v218, v222
	s_branch .LBB0_1089
